# s20
# baseline (speedup 1.0000x reference)
.LBB0_3:
	s_cmpk_gt_u32 s10, 0x17f
	s_cbranch_scc0 .LBB0_7
	s_load_dwordx2 s[4:5], s[0:1], 0x0
	s_load_dwordx2 s[6:7], s[0:1], 0x18
	s_load_dwordx2 s[12:13], s[0:1], 0x20
	s_load_dwordx2 s[14:15], s[0:1], 0x38
	s_sub_i32 s8, s10, 0x180
	s_lshr_b32 s2, s8, 1
	s_and_b32 s3, s8, 1
	s_lshl_b32 s9, s2, 5
	s_lshl_b32 s11, s2, 15
	s_lshl_b32 s3, s3, 16
	v_and_b32_e32 v1, 63, v0
	v_lshrrev_b32_e32 v2, 6, v0
	v_lshlrev_b32_e32 v1, 6, v1
	v_add_u32_e32 v4, s11, v1
	v_lshl_add_u32 v3, v2, 14, v1
	v_add_u32_e32 v3, s3, v3
	v_lshlrev_b32_e32 v10, 14, v2
	v_add_u32_e32 v10, s3, v10
	s_waitcnt lgkmcnt(0)
	s_load_dwordx8 s[16:23], s[12:13], s9
	v_add_u32_e32 v10, s9, v10
	global_load_dwordx4 v[12:15], v4, s[6:7]
	global_load_dwordx4 v[16:19], v4, s[6:7] offset:16
	global_load_dwordx4 v[20:23], v4, s[6:7] offset:32
	global_load_dwordx4 v[24:27], v4, s[6:7] offset:48
	v_add_u32_e32 v6, 0x1000, v4
	global_load_dwordx4 v[28:31], v6, s[6:7]
	global_load_dwordx4 v[32:35], v6, s[6:7] offset:16
	global_load_dwordx4 v[36:39], v6, s[6:7] offset:32
	global_load_dwordx4 v[40:43], v6, s[6:7] offset:48
	v_add_u32_e32 v5, 0x2000, v4
	global_load_dwordx4 v[44:47], v5, s[6:7]
	global_load_dwordx4 v[48:51], v5, s[6:7] offset:16
	global_load_dwordx4 v[52:55], v5, s[6:7] offset:32
	global_load_dwordx4 v[56:59], v5, s[6:7] offset:48
	v_add_u32_e32 v6, 0x3000, v4
	global_load_dwordx4 v[60:63], v6, s[6:7]
	global_load_dwordx4 v[64:67], v6, s[6:7] offset:16
	global_load_dwordx4 v[68:71], v6, s[6:7] offset:32
	global_load_dwordx4 v[72:75], v6, s[6:7] offset:48
	v_add_u32_e32 v5, 0x4000, v4
	global_load_dwordx4 v[76:79], v5, s[6:7]
	global_load_dwordx4 v[80:83], v5, s[6:7] offset:16
	global_load_dwordx4 v[84:87], v5, s[6:7] offset:32
	global_load_dwordx4 v[88:91], v5, s[6:7] offset:48
	v_add_u32_e32 v6, 0x5000, v4
	global_load_dwordx4 v[92:95], v6, s[6:7]
	global_load_dwordx4 v[96:99], v6, s[6:7] offset:16
	global_load_dwordx4 v[100:103], v6, s[6:7] offset:32
	global_load_dwordx4 v[104:107], v6, s[6:7] offset:48
	v_add_u32_e32 v5, 0x6000, v4
	global_load_dwordx4 v[108:111], v5, s[6:7]
	global_load_dwordx4 v[112:115], v5, s[6:7] offset:16
	global_load_dwordx4 v[116:119], v5, s[6:7] offset:32
	global_load_dwordx4 v[120:123], v5, s[6:7] offset:48
	v_add_u32_e32 v6, 0x7000, v4
	global_load_dwordx4 v[124:127], v6, s[6:7]
	global_load_dwordx4 v[128:131], v6, s[6:7] offset:16
	global_load_dwordx4 v[132:135], v6, s[6:7] offset:32
	global_load_dwordx4 v[136:139], v6, s[6:7] offset:48
	global_load_dwordx4 v[140:143], v3, s[4:5]
	global_load_dwordx4 v[144:147], v3, s[4:5] offset:16
	global_load_dwordx4 v[148:151], v3, s[4:5] offset:32
	global_load_dwordx4 v[152:155], v3, s[4:5] offset:48
	v_add_u32_e32 v9, 0x1000, v3
	global_load_dwordx4 v[156:159], v9, s[4:5]
	global_load_dwordx4 v[160:163], v9, s[4:5] offset:16
	global_load_dwordx4 v[164:167], v9, s[4:5] offset:32
	global_load_dwordx4 v[168:171], v9, s[4:5] offset:48
	v_add_u32_e32 v8, 0x2000, v3
	global_load_dwordx4 v[172:175], v8, s[4:5]
	global_load_dwordx4 v[176:179], v8, s[4:5] offset:16
	global_load_dwordx4 v[180:183], v8, s[4:5] offset:32
	global_load_dwordx4 v[184:187], v8, s[4:5] offset:48
	v_add_u32_e32 v9, 0x3000, v3
	global_load_dwordx4 v[188:191], v9, s[4:5]
	global_load_dwordx4 v[192:195], v9, s[4:5] offset:16
	global_load_dwordx4 v[196:199], v9, s[4:5] offset:32
	global_load_dwordx4 v[200:203], v9, s[4:5] offset:48
	s_waitcnt vmcnt(12)
	v_mul_f32_e32 v204, v12, v140
	v_mul_f32_e32 v205, v28, v140
	v_mul_f32_e32 v206, v44, v140
	v_mul_f32_e32 v207, v60, v140
	v_mul_f32_e32 v208, v76, v140
	v_mul_f32_e32 v209, v92, v140
	v_mul_f32_e32 v210, v108, v140
	v_mul_f32_e32 v211, v124, v140
	v_fmac_f32_e32 v204, v13, v141
	v_fmac_f32_e32 v205, v29, v141
	v_fmac_f32_e32 v206, v45, v141
	v_fmac_f32_e32 v207, v61, v141
	v_fmac_f32_e32 v208, v77, v141
	v_fmac_f32_e32 v209, v93, v141
	v_fmac_f32_e32 v210, v109, v141
	v_fmac_f32_e32 v211, v125, v141
	v_fmac_f32_e32 v204, v14, v142
	v_fmac_f32_e32 v205, v30, v142
	v_fmac_f32_e32 v206, v46, v142
	v_fmac_f32_e32 v207, v62, v142
	v_fmac_f32_e32 v208, v78, v142
	v_fmac_f32_e32 v209, v94, v142
	v_fmac_f32_e32 v210, v110, v142
	v_fmac_f32_e32 v211, v126, v142
	v_fmac_f32_e32 v204, v15, v143
	v_fmac_f32_e32 v205, v31, v143
	v_fmac_f32_e32 v206, v47, v143
	v_fmac_f32_e32 v207, v63, v143
	v_fmac_f32_e32 v208, v79, v143
	v_fmac_f32_e32 v209, v95, v143
	v_fmac_f32_e32 v210, v111, v143
	v_fmac_f32_e32 v211, v127, v143
	v_fmac_f32_e32 v204, v16, v144
	v_fmac_f32_e32 v205, v32, v144
	v_fmac_f32_e32 v206, v48, v144
	v_fmac_f32_e32 v207, v64, v144
	v_fmac_f32_e32 v208, v80, v144
	v_fmac_f32_e32 v209, v96, v144
	v_fmac_f32_e32 v210, v112, v144
	v_fmac_f32_e32 v211, v128, v144
	v_fmac_f32_e32 v204, v17, v145
	v_fmac_f32_e32 v205, v33, v145
	v_fmac_f32_e32 v206, v49, v145
	v_fmac_f32_e32 v207, v65, v145
	v_fmac_f32_e32 v208, v81, v145
	v_fmac_f32_e32 v209, v97, v145
	v_fmac_f32_e32 v210, v113, v145
	v_fmac_f32_e32 v211, v129, v145
	v_fmac_f32_e32 v204, v18, v146
	v_fmac_f32_e32 v205, v34, v146
	v_fmac_f32_e32 v206, v50, v146
	v_fmac_f32_e32 v207, v66, v146
	v_fmac_f32_e32 v208, v82, v146
	v_fmac_f32_e32 v209, v98, v146
	v_fmac_f32_e32 v210, v114, v146
	v_fmac_f32_e32 v211, v130, v146
	v_fmac_f32_e32 v204, v19, v147
	v_fmac_f32_e32 v205, v35, v147
	v_fmac_f32_e32 v206, v51, v147
	v_fmac_f32_e32 v207, v67, v147
	v_fmac_f32_e32 v208, v83, v147
	v_fmac_f32_e32 v209, v99, v147
	v_fmac_f32_e32 v210, v115, v147
	v_fmac_f32_e32 v211, v131, v147
	v_fmac_f32_e32 v204, v20, v148
	v_fmac_f32_e32 v205, v36, v148
	v_fmac_f32_e32 v206, v52, v148
	v_fmac_f32_e32 v207, v68, v148
	v_fmac_f32_e32 v208, v84, v148
	v_fmac_f32_e32 v209, v100, v148
	v_fmac_f32_e32 v210, v116, v148
	v_fmac_f32_e32 v211, v132, v148
	v_fmac_f32_e32 v204, v21, v149
	v_fmac_f32_e32 v205, v37, v149
	v_fmac_f32_e32 v206, v53, v149
	v_fmac_f32_e32 v207, v69, v149
	v_fmac_f32_e32 v208, v85, v149
	v_fmac_f32_e32 v209, v101, v149
	v_fmac_f32_e32 v210, v117, v149
	v_fmac_f32_e32 v211, v133, v149
	v_fmac_f32_e32 v204, v22, v150
	v_fmac_f32_e32 v205, v38, v150
	v_fmac_f32_e32 v206, v54, v150
	v_fmac_f32_e32 v207, v70, v150
	v_fmac_f32_e32 v208, v86, v150
	v_fmac_f32_e32 v209, v102, v150
	v_fmac_f32_e32 v210, v118, v150
	v_fmac_f32_e32 v211, v134, v150
	v_fmac_f32_e32 v204, v23, v151
	v_fmac_f32_e32 v205, v39, v151
	v_fmac_f32_e32 v206, v55, v151
	v_fmac_f32_e32 v207, v71, v151
	v_fmac_f32_e32 v208, v87, v151
	v_fmac_f32_e32 v209, v103, v151
	v_fmac_f32_e32 v210, v119, v151
	v_fmac_f32_e32 v211, v135, v151
	v_fmac_f32_e32 v204, v24, v152
	v_fmac_f32_e32 v205, v40, v152
	v_fmac_f32_e32 v206, v56, v152
	v_fmac_f32_e32 v207, v72, v152
	v_fmac_f32_e32 v208, v88, v152
	v_fmac_f32_e32 v209, v104, v152
	v_fmac_f32_e32 v210, v120, v152
	v_fmac_f32_e32 v211, v136, v152
	v_fmac_f32_e32 v204, v25, v153
	v_fmac_f32_e32 v205, v41, v153
	v_fmac_f32_e32 v206, v57, v153
	v_fmac_f32_e32 v207, v73, v153
	v_fmac_f32_e32 v208, v89, v153
	v_fmac_f32_e32 v209, v105, v153
	v_fmac_f32_e32 v210, v121, v153
	v_fmac_f32_e32 v211, v137, v153
	v_fmac_f32_e32 v204, v26, v154
	v_fmac_f32_e32 v205, v42, v154
	v_fmac_f32_e32 v206, v58, v154
	v_fmac_f32_e32 v207, v74, v154
	v_fmac_f32_e32 v208, v90, v154
	v_fmac_f32_e32 v209, v106, v154
	v_fmac_f32_e32 v210, v122, v154
	v_fmac_f32_e32 v211, v138, v154
	v_fmac_f32_e32 v204, v27, v155
	v_fmac_f32_e32 v205, v43, v155
	v_fmac_f32_e32 v206, v59, v155
	v_fmac_f32_e32 v207, v75, v155
	v_fmac_f32_e32 v208, v91, v155
	v_fmac_f32_e32 v209, v107, v155
	v_fmac_f32_e32 v210, v123, v155
	v_fmac_f32_e32 v211, v139, v155
	s_nop 1
	v_add_f32_dpp v204, v204, v204 quad_perm:[1,0,3,2] row_mask:0xf bank_mask:0xf
	v_add_f32_dpp v205, v205, v205 quad_perm:[1,0,3,2] row_mask:0xf bank_mask:0xf
	v_add_f32_dpp v206, v206, v206 quad_perm:[1,0,3,2] row_mask:0xf bank_mask:0xf
	v_add_f32_dpp v207, v207, v207 quad_perm:[1,0,3,2] row_mask:0xf bank_mask:0xf
	v_add_f32_dpp v208, v208, v208 quad_perm:[1,0,3,2] row_mask:0xf bank_mask:0xf
	v_add_f32_dpp v209, v209, v209 quad_perm:[1,0,3,2] row_mask:0xf bank_mask:0xf
	v_add_f32_dpp v210, v210, v210 quad_perm:[1,0,3,2] row_mask:0xf bank_mask:0xf
	v_add_f32_dpp v211, v211, v211 quad_perm:[1,0,3,2] row_mask:0xf bank_mask:0xf
	v_add_f32_dpp v204, v204, v204 quad_perm:[2,3,0,1] row_mask:0xf bank_mask:0xf
	v_add_f32_dpp v205, v205, v205 quad_perm:[2,3,0,1] row_mask:0xf bank_mask:0xf
	v_add_f32_dpp v206, v206, v206 quad_perm:[2,3,0,1] row_mask:0xf bank_mask:0xf
	v_add_f32_dpp v207, v207, v207 quad_perm:[2,3,0,1] row_mask:0xf bank_mask:0xf
	v_add_f32_dpp v208, v208, v208 quad_perm:[2,3,0,1] row_mask:0xf bank_mask:0xf
	v_add_f32_dpp v209, v209, v209 quad_perm:[2,3,0,1] row_mask:0xf bank_mask:0xf
	v_add_f32_dpp v210, v210, v210 quad_perm:[2,3,0,1] row_mask:0xf bank_mask:0xf
	v_add_f32_dpp v211, v211, v211 quad_perm:[2,3,0,1] row_mask:0xf bank_mask:0xf
	v_add_f32_dpp v204, v204, v204 row_half_mirror row_mask:0xf bank_mask:0xf
	v_add_f32_dpp v205, v205, v205 row_half_mirror row_mask:0xf bank_mask:0xf
	v_add_f32_dpp v206, v206, v206 row_half_mirror row_mask:0xf bank_mask:0xf
	v_add_f32_dpp v207, v207, v207 row_half_mirror row_mask:0xf bank_mask:0xf
	v_add_f32_dpp v208, v208, v208 row_half_mirror row_mask:0xf bank_mask:0xf
	v_add_f32_dpp v209, v209, v209 row_half_mirror row_mask:0xf bank_mask:0xf
	v_add_f32_dpp v210, v210, v210 row_half_mirror row_mask:0xf bank_mask:0xf
	v_add_f32_dpp v211, v211, v211 row_half_mirror row_mask:0xf bank_mask:0xf
	v_add_f32_dpp v204, v204, v204 row_mirror row_mask:0xf bank_mask:0xf
	v_add_f32_dpp v205, v205, v205 row_mirror row_mask:0xf bank_mask:0xf
	v_add_f32_dpp v206, v206, v206 row_mirror row_mask:0xf bank_mask:0xf
	v_add_f32_dpp v207, v207, v207 row_mirror row_mask:0xf bank_mask:0xf
	v_add_f32_dpp v208, v208, v208 row_mirror row_mask:0xf bank_mask:0xf
	v_add_f32_dpp v209, v209, v209 row_mirror row_mask:0xf bank_mask:0xf
	v_add_f32_dpp v210, v210, v210 row_mirror row_mask:0xf bank_mask:0xf
	v_add_f32_dpp v211, v211, v211 row_mirror row_mask:0xf bank_mask:0xf
	v_add_f32_dpp v204, v204, v204 row_bcast:15 row_mask:0xa bank_mask:0xf
	v_add_f32_dpp v205, v205, v205 row_bcast:15 row_mask:0xa bank_mask:0xf
	v_add_f32_dpp v206, v206, v206 row_bcast:15 row_mask:0xa bank_mask:0xf
	v_add_f32_dpp v207, v207, v207 row_bcast:15 row_mask:0xa bank_mask:0xf
	v_add_f32_dpp v208, v208, v208 row_bcast:15 row_mask:0xa bank_mask:0xf
	v_add_f32_dpp v209, v209, v209 row_bcast:15 row_mask:0xa bank_mask:0xf
	v_add_f32_dpp v210, v210, v210 row_bcast:15 row_mask:0xa bank_mask:0xf
	v_add_f32_dpp v211, v211, v211 row_bcast:15 row_mask:0xa bank_mask:0xf
	v_add_f32_dpp v204, v204, v204 row_bcast:31 row_mask:0xc bank_mask:0xf
	v_add_f32_dpp v205, v205, v205 row_bcast:31 row_mask:0xc bank_mask:0xf
	v_add_f32_dpp v206, v206, v206 row_bcast:31 row_mask:0xc bank_mask:0xf
	v_add_f32_dpp v207, v207, v207 row_bcast:31 row_mask:0xc bank_mask:0xf
	v_add_f32_dpp v208, v208, v208 row_bcast:31 row_mask:0xc bank_mask:0xf
	v_add_f32_dpp v209, v209, v209 row_bcast:31 row_mask:0xc bank_mask:0xf
	v_add_f32_dpp v210, v210, v210 row_bcast:31 row_mask:0xc bank_mask:0xf
	v_add_f32_dpp v211, v211, v211 row_bcast:31 row_mask:0xc bank_mask:0xf
	s_waitcnt vmcnt(8)
	v_mul_f32_e32 v212, v12, v156
	v_mul_f32_e32 v213, v28, v156
	v_mul_f32_e32 v214, v44, v156
	v_mul_f32_e32 v215, v60, v156
	v_mul_f32_e32 v216, v76, v156
	v_mul_f32_e32 v217, v92, v156
	v_mul_f32_e32 v218, v108, v156
	v_mul_f32_e32 v219, v124, v156
	v_fmac_f32_e32 v212, v13, v157
	v_fmac_f32_e32 v213, v29, v157
	v_fmac_f32_e32 v214, v45, v157
	v_fmac_f32_e32 v215, v61, v157
	v_fmac_f32_e32 v216, v77, v157
	v_fmac_f32_e32 v217, v93, v157
	v_fmac_f32_e32 v218, v109, v157
	v_fmac_f32_e32 v219, v125, v157
	v_fmac_f32_e32 v212, v14, v158
	v_fmac_f32_e32 v213, v30, v158
	v_fmac_f32_e32 v214, v46, v158
	v_fmac_f32_e32 v215, v62, v158
	v_fmac_f32_e32 v216, v78, v158
	v_fmac_f32_e32 v217, v94, v158
	v_fmac_f32_e32 v218, v110, v158
	v_fmac_f32_e32 v219, v126, v158
	v_fmac_f32_e32 v212, v15, v159
	v_fmac_f32_e32 v213, v31, v159
	v_fmac_f32_e32 v214, v47, v159
	v_fmac_f32_e32 v215, v63, v159
	v_fmac_f32_e32 v216, v79, v159
	v_fmac_f32_e32 v217, v95, v159
	v_fmac_f32_e32 v218, v111, v159
	v_fmac_f32_e32 v219, v127, v159
	v_fmac_f32_e32 v212, v16, v160
	v_fmac_f32_e32 v213, v32, v160
	v_fmac_f32_e32 v214, v48, v160
	v_fmac_f32_e32 v215, v64, v160
	v_fmac_f32_e32 v216, v80, v160
	v_fmac_f32_e32 v217, v96, v160
	v_fmac_f32_e32 v218, v112, v160
	v_fmac_f32_e32 v219, v128, v160
	v_fmac_f32_e32 v212, v17, v161
	v_fmac_f32_e32 v213, v33, v161
	v_fmac_f32_e32 v214, v49, v161
	v_fmac_f32_e32 v215, v65, v161
	v_fmac_f32_e32 v216, v81, v161
	v_fmac_f32_e32 v217, v97, v161
	v_fmac_f32_e32 v218, v113, v161
	v_fmac_f32_e32 v219, v129, v161
	v_fmac_f32_e32 v212, v18, v162
	v_fmac_f32_e32 v213, v34, v162
	v_fmac_f32_e32 v214, v50, v162
	v_fmac_f32_e32 v215, v66, v162
	v_fmac_f32_e32 v216, v82, v162
	v_fmac_f32_e32 v217, v98, v162
	v_fmac_f32_e32 v218, v114, v162
	v_fmac_f32_e32 v219, v130, v162
	v_fmac_f32_e32 v212, v19, v163
	v_fmac_f32_e32 v213, v35, v163
	v_fmac_f32_e32 v214, v51, v163
	v_fmac_f32_e32 v215, v67, v163
	v_fmac_f32_e32 v216, v83, v163
	v_fmac_f32_e32 v217, v99, v163
	v_fmac_f32_e32 v218, v115, v163
	v_fmac_f32_e32 v219, v131, v163
	v_fmac_f32_e32 v212, v20, v164
	v_fmac_f32_e32 v213, v36, v164
	v_fmac_f32_e32 v214, v52, v164
	v_fmac_f32_e32 v215, v68, v164
	v_fmac_f32_e32 v216, v84, v164
	v_fmac_f32_e32 v217, v100, v164
	v_fmac_f32_e32 v218, v116, v164
	v_fmac_f32_e32 v219, v132, v164
	v_fmac_f32_e32 v212, v21, v165
	v_fmac_f32_e32 v213, v37, v165
	v_fmac_f32_e32 v214, v53, v165
	v_fmac_f32_e32 v215, v69, v165
	v_fmac_f32_e32 v216, v85, v165
	v_fmac_f32_e32 v217, v101, v165
	v_fmac_f32_e32 v218, v117, v165
	v_fmac_f32_e32 v219, v133, v165
	v_fmac_f32_e32 v212, v22, v166
	v_fmac_f32_e32 v213, v38, v166
	v_fmac_f32_e32 v214, v54, v166
	v_fmac_f32_e32 v215, v70, v166
	v_fmac_f32_e32 v216, v86, v166
	v_fmac_f32_e32 v217, v102, v166
	v_fmac_f32_e32 v218, v118, v166
	v_fmac_f32_e32 v219, v134, v166
	v_fmac_f32_e32 v212, v23, v167
	v_fmac_f32_e32 v213, v39, v167
	v_fmac_f32_e32 v214, v55, v167
	v_fmac_f32_e32 v215, v71, v167
	v_fmac_f32_e32 v216, v87, v167
	v_fmac_f32_e32 v217, v103, v167
	v_fmac_f32_e32 v218, v119, v167
	v_fmac_f32_e32 v219, v135, v167
	v_fmac_f32_e32 v212, v24, v168
	v_fmac_f32_e32 v213, v40, v168
	v_fmac_f32_e32 v214, v56, v168
	v_fmac_f32_e32 v215, v72, v168
	v_fmac_f32_e32 v216, v88, v168
	v_fmac_f32_e32 v217, v104, v168
	v_fmac_f32_e32 v218, v120, v168
	v_fmac_f32_e32 v219, v136, v168
	v_fmac_f32_e32 v212, v25, v169
	v_fmac_f32_e32 v213, v41, v169
	v_fmac_f32_e32 v214, v57, v169
	v_fmac_f32_e32 v215, v73, v169
	v_fmac_f32_e32 v216, v89, v169
	v_fmac_f32_e32 v217, v105, v169
	v_fmac_f32_e32 v218, v121, v169
	v_fmac_f32_e32 v219, v137, v169
	v_fmac_f32_e32 v212, v26, v170
	v_fmac_f32_e32 v213, v42, v170
	v_fmac_f32_e32 v214, v58, v170
	v_fmac_f32_e32 v215, v74, v170
	v_fmac_f32_e32 v216, v90, v170
	v_fmac_f32_e32 v217, v106, v170
	v_fmac_f32_e32 v218, v122, v170
	v_fmac_f32_e32 v219, v138, v170
	v_fmac_f32_e32 v212, v27, v171
	v_fmac_f32_e32 v213, v43, v171
	v_fmac_f32_e32 v214, v59, v171
	v_fmac_f32_e32 v215, v75, v171
	v_fmac_f32_e32 v216, v91, v171
	v_fmac_f32_e32 v217, v107, v171
	v_fmac_f32_e32 v218, v123, v171
	v_fmac_f32_e32 v219, v139, v171
	s_nop 1
	v_add_f32_dpp v212, v212, v212 quad_perm:[1,0,3,2] row_mask:0xf bank_mask:0xf
	v_add_f32_dpp v213, v213, v213 quad_perm:[1,0,3,2] row_mask:0xf bank_mask:0xf
	v_add_f32_dpp v214, v214, v214 quad_perm:[1,0,3,2] row_mask:0xf bank_mask:0xf
	v_add_f32_dpp v215, v215, v215 quad_perm:[1,0,3,2] row_mask:0xf bank_mask:0xf
	v_add_f32_dpp v216, v216, v216 quad_perm:[1,0,3,2] row_mask:0xf bank_mask:0xf
	v_add_f32_dpp v217, v217, v217 quad_perm:[1,0,3,2] row_mask:0xf bank_mask:0xf
	v_add_f32_dpp v218, v218, v218 quad_perm:[1,0,3,2] row_mask:0xf bank_mask:0xf
	v_add_f32_dpp v219, v219, v219 quad_perm:[1,0,3,2] row_mask:0xf bank_mask:0xf
	v_add_f32_dpp v212, v212, v212 quad_perm:[2,3,0,1] row_mask:0xf bank_mask:0xf
	v_add_f32_dpp v213, v213, v213 quad_perm:[2,3,0,1] row_mask:0xf bank_mask:0xf
	v_add_f32_dpp v214, v214, v214 quad_perm:[2,3,0,1] row_mask:0xf bank_mask:0xf
	v_add_f32_dpp v215, v215, v215 quad_perm:[2,3,0,1] row_mask:0xf bank_mask:0xf
	v_add_f32_dpp v216, v216, v216 quad_perm:[2,3,0,1] row_mask:0xf bank_mask:0xf
	v_add_f32_dpp v217, v217, v217 quad_perm:[2,3,0,1] row_mask:0xf bank_mask:0xf
	v_add_f32_dpp v218, v218, v218 quad_perm:[2,3,0,1] row_mask:0xf bank_mask:0xf
	v_add_f32_dpp v219, v219, v219 quad_perm:[2,3,0,1] row_mask:0xf bank_mask:0xf
	v_add_f32_dpp v212, v212, v212 row_half_mirror row_mask:0xf bank_mask:0xf
	v_add_f32_dpp v213, v213, v213 row_half_mirror row_mask:0xf bank_mask:0xf
	v_add_f32_dpp v214, v214, v214 row_half_mirror row_mask:0xf bank_mask:0xf
	v_add_f32_dpp v215, v215, v215 row_half_mirror row_mask:0xf bank_mask:0xf
	v_add_f32_dpp v216, v216, v216 row_half_mirror row_mask:0xf bank_mask:0xf
	v_add_f32_dpp v217, v217, v217 row_half_mirror row_mask:0xf bank_mask:0xf
	v_add_f32_dpp v218, v218, v218 row_half_mirror row_mask:0xf bank_mask:0xf
	v_add_f32_dpp v219, v219, v219 row_half_mirror row_mask:0xf bank_mask:0xf
	v_add_f32_dpp v212, v212, v212 row_mirror row_mask:0xf bank_mask:0xf
	v_add_f32_dpp v213, v213, v213 row_mirror row_mask:0xf bank_mask:0xf
	v_add_f32_dpp v214, v214, v214 row_mirror row_mask:0xf bank_mask:0xf
	v_add_f32_dpp v215, v215, v215 row_mirror row_mask:0xf bank_mask:0xf
	v_add_f32_dpp v216, v216, v216 row_mirror row_mask:0xf bank_mask:0xf
	v_add_f32_dpp v217, v217, v217 row_mirror row_mask:0xf bank_mask:0xf
	v_add_f32_dpp v218, v218, v218 row_mirror row_mask:0xf bank_mask:0xf
	v_add_f32_dpp v219, v219, v219 row_mirror row_mask:0xf bank_mask:0xf
	v_add_f32_dpp v212, v212, v212 row_bcast:15 row_mask:0xa bank_mask:0xf
	v_add_f32_dpp v213, v213, v213 row_bcast:15 row_mask:0xa bank_mask:0xf
	v_add_f32_dpp v214, v214, v214 row_bcast:15 row_mask:0xa bank_mask:0xf
	v_add_f32_dpp v215, v215, v215 row_bcast:15 row_mask:0xa bank_mask:0xf
	v_add_f32_dpp v216, v216, v216 row_bcast:15 row_mask:0xa bank_mask:0xf
	v_add_f32_dpp v217, v217, v217 row_bcast:15 row_mask:0xa bank_mask:0xf
	v_add_f32_dpp v218, v218, v218 row_bcast:15 row_mask:0xa bank_mask:0xf
	v_add_f32_dpp v219, v219, v219 row_bcast:15 row_mask:0xa bank_mask:0xf
	v_add_f32_dpp v212, v212, v212 row_bcast:31 row_mask:0xc bank_mask:0xf
	v_add_f32_dpp v213, v213, v213 row_bcast:31 row_mask:0xc bank_mask:0xf
	v_add_f32_dpp v214, v214, v214 row_bcast:31 row_mask:0xc bank_mask:0xf
	v_add_f32_dpp v215, v215, v215 row_bcast:31 row_mask:0xc bank_mask:0xf
	v_add_f32_dpp v216, v216, v216 row_bcast:31 row_mask:0xc bank_mask:0xf
	v_add_f32_dpp v217, v217, v217 row_bcast:31 row_mask:0xc bank_mask:0xf
	v_add_f32_dpp v218, v218, v218 row_bcast:31 row_mask:0xc bank_mask:0xf
	v_add_f32_dpp v219, v219, v219 row_bcast:31 row_mask:0xc bank_mask:0xf
	s_waitcnt vmcnt(4)
	v_mul_f32_e32 v220, v12, v172
	v_mul_f32_e32 v221, v28, v172
	v_mul_f32_e32 v222, v44, v172
	v_mul_f32_e32 v223, v60, v172
	v_mul_f32_e32 v224, v76, v172
	v_mul_f32_e32 v225, v92, v172
	v_mul_f32_e32 v226, v108, v172
	v_mul_f32_e32 v227, v124, v172
	v_fmac_f32_e32 v220, v13, v173
	v_fmac_f32_e32 v221, v29, v173
	v_fmac_f32_e32 v222, v45, v173
	v_fmac_f32_e32 v223, v61, v173
	v_fmac_f32_e32 v224, v77, v173
	v_fmac_f32_e32 v225, v93, v173
	v_fmac_f32_e32 v226, v109, v173
	v_fmac_f32_e32 v227, v125, v173
	v_fmac_f32_e32 v220, v14, v174
	v_fmac_f32_e32 v221, v30, v174
	v_fmac_f32_e32 v222, v46, v174
	v_fmac_f32_e32 v223, v62, v174
	v_fmac_f32_e32 v224, v78, v174
	v_fmac_f32_e32 v225, v94, v174
	v_fmac_f32_e32 v226, v110, v174
	v_fmac_f32_e32 v227, v126, v174
	v_fmac_f32_e32 v220, v15, v175
	v_fmac_f32_e32 v221, v31, v175
	v_fmac_f32_e32 v222, v47, v175
	v_fmac_f32_e32 v223, v63, v175
	v_fmac_f32_e32 v224, v79, v175
	v_fmac_f32_e32 v225, v95, v175
	v_fmac_f32_e32 v226, v111, v175
	v_fmac_f32_e32 v227, v127, v175
	v_fmac_f32_e32 v220, v16, v176
	v_fmac_f32_e32 v221, v32, v176
	v_fmac_f32_e32 v222, v48, v176
	v_fmac_f32_e32 v223, v64, v176
	v_fmac_f32_e32 v224, v80, v176
	v_fmac_f32_e32 v225, v96, v176
	v_fmac_f32_e32 v226, v112, v176
	v_fmac_f32_e32 v227, v128, v176
	v_fmac_f32_e32 v220, v17, v177
	v_fmac_f32_e32 v221, v33, v177
	v_fmac_f32_e32 v222, v49, v177
	v_fmac_f32_e32 v223, v65, v177
	v_fmac_f32_e32 v224, v81, v177
	v_fmac_f32_e32 v225, v97, v177
	v_fmac_f32_e32 v226, v113, v177
	v_fmac_f32_e32 v227, v129, v177
	v_fmac_f32_e32 v220, v18, v178
	v_fmac_f32_e32 v221, v34, v178
	v_fmac_f32_e32 v222, v50, v178
	v_fmac_f32_e32 v223, v66, v178
	v_fmac_f32_e32 v224, v82, v178
	v_fmac_f32_e32 v225, v98, v178
	v_fmac_f32_e32 v226, v114, v178
	v_fmac_f32_e32 v227, v130, v178
	v_fmac_f32_e32 v220, v19, v179
	v_fmac_f32_e32 v221, v35, v179
	v_fmac_f32_e32 v222, v51, v179
	v_fmac_f32_e32 v223, v67, v179
	v_fmac_f32_e32 v224, v83, v179
	v_fmac_f32_e32 v225, v99, v179
	v_fmac_f32_e32 v226, v115, v179
	v_fmac_f32_e32 v227, v131, v179
	v_fmac_f32_e32 v220, v20, v180
	v_fmac_f32_e32 v221, v36, v180
	v_fmac_f32_e32 v222, v52, v180
	v_fmac_f32_e32 v223, v68, v180
	v_fmac_f32_e32 v224, v84, v180
	v_fmac_f32_e32 v225, v100, v180
	v_fmac_f32_e32 v226, v116, v180
	v_fmac_f32_e32 v227, v132, v180
	v_fmac_f32_e32 v220, v21, v181
	v_fmac_f32_e32 v221, v37, v181
	v_fmac_f32_e32 v222, v53, v181
	v_fmac_f32_e32 v223, v69, v181
	v_fmac_f32_e32 v224, v85, v181
	v_fmac_f32_e32 v225, v101, v181
	v_fmac_f32_e32 v226, v117, v181
	v_fmac_f32_e32 v227, v133, v181
	v_fmac_f32_e32 v220, v22, v182
	v_fmac_f32_e32 v221, v38, v182
	v_fmac_f32_e32 v222, v54, v182
	v_fmac_f32_e32 v223, v70, v182
	v_fmac_f32_e32 v224, v86, v182
	v_fmac_f32_e32 v225, v102, v182
	v_fmac_f32_e32 v226, v118, v182
	v_fmac_f32_e32 v227, v134, v182
	v_fmac_f32_e32 v220, v23, v183
	v_fmac_f32_e32 v221, v39, v183
	v_fmac_f32_e32 v222, v55, v183
	v_fmac_f32_e32 v223, v71, v183
	v_fmac_f32_e32 v224, v87, v183
	v_fmac_f32_e32 v225, v103, v183
	v_fmac_f32_e32 v226, v119, v183
	v_fmac_f32_e32 v227, v135, v183
	v_fmac_f32_e32 v220, v24, v184
	v_fmac_f32_e32 v221, v40, v184
	v_fmac_f32_e32 v222, v56, v184
	v_fmac_f32_e32 v223, v72, v184
	v_fmac_f32_e32 v224, v88, v184
	v_fmac_f32_e32 v225, v104, v184
	v_fmac_f32_e32 v226, v120, v184
	v_fmac_f32_e32 v227, v136, v184
	v_fmac_f32_e32 v220, v25, v185
	v_fmac_f32_e32 v221, v41, v185
	v_fmac_f32_e32 v222, v57, v185
	v_fmac_f32_e32 v223, v73, v185
	v_fmac_f32_e32 v224, v89, v185
	v_fmac_f32_e32 v225, v105, v185
	v_fmac_f32_e32 v226, v121, v185
	v_fmac_f32_e32 v227, v137, v185
	v_fmac_f32_e32 v220, v26, v186
	v_fmac_f32_e32 v221, v42, v186
	v_fmac_f32_e32 v222, v58, v186
	v_fmac_f32_e32 v223, v74, v186
	v_fmac_f32_e32 v224, v90, v186
	v_fmac_f32_e32 v225, v106, v186
	v_fmac_f32_e32 v226, v122, v186
	v_fmac_f32_e32 v227, v138, v186
	v_fmac_f32_e32 v220, v27, v187
	v_fmac_f32_e32 v221, v43, v187
	v_fmac_f32_e32 v222, v59, v187
	v_fmac_f32_e32 v223, v75, v187
	v_fmac_f32_e32 v224, v91, v187
	v_fmac_f32_e32 v225, v107, v187
	v_fmac_f32_e32 v226, v123, v187
	v_fmac_f32_e32 v227, v139, v187
	s_nop 1
	v_add_f32_dpp v220, v220, v220 quad_perm:[1,0,3,2] row_mask:0xf bank_mask:0xf
	v_add_f32_dpp v221, v221, v221 quad_perm:[1,0,3,2] row_mask:0xf bank_mask:0xf
	v_add_f32_dpp v222, v222, v222 quad_perm:[1,0,3,2] row_mask:0xf bank_mask:0xf
	v_add_f32_dpp v223, v223, v223 quad_perm:[1,0,3,2] row_mask:0xf bank_mask:0xf
	v_add_f32_dpp v224, v224, v224 quad_perm:[1,0,3,2] row_mask:0xf bank_mask:0xf
	v_add_f32_dpp v225, v225, v225 quad_perm:[1,0,3,2] row_mask:0xf bank_mask:0xf
	v_add_f32_dpp v226, v226, v226 quad_perm:[1,0,3,2] row_mask:0xf bank_mask:0xf
	v_add_f32_dpp v227, v227, v227 quad_perm:[1,0,3,2] row_mask:0xf bank_mask:0xf
	v_add_f32_dpp v220, v220, v220 quad_perm:[2,3,0,1] row_mask:0xf bank_mask:0xf
	v_add_f32_dpp v221, v221, v221 quad_perm:[2,3,0,1] row_mask:0xf bank_mask:0xf
	v_add_f32_dpp v222, v222, v222 quad_perm:[2,3,0,1] row_mask:0xf bank_mask:0xf
	v_add_f32_dpp v223, v223, v223 quad_perm:[2,3,0,1] row_mask:0xf bank_mask:0xf
	v_add_f32_dpp v224, v224, v224 quad_perm:[2,3,0,1] row_mask:0xf bank_mask:0xf
	v_add_f32_dpp v225, v225, v225 quad_perm:[2,3,0,1] row_mask:0xf bank_mask:0xf
	v_add_f32_dpp v226, v226, v226 quad_perm:[2,3,0,1] row_mask:0xf bank_mask:0xf
	v_add_f32_dpp v227, v227, v227 quad_perm:[2,3,0,1] row_mask:0xf bank_mask:0xf
	v_add_f32_dpp v220, v220, v220 row_half_mirror row_mask:0xf bank_mask:0xf
	v_add_f32_dpp v221, v221, v221 row_half_mirror row_mask:0xf bank_mask:0xf
	v_add_f32_dpp v222, v222, v222 row_half_mirror row_mask:0xf bank_mask:0xf
	v_add_f32_dpp v223, v223, v223 row_half_mirror row_mask:0xf bank_mask:0xf
	v_add_f32_dpp v224, v224, v224 row_half_mirror row_mask:0xf bank_mask:0xf
	v_add_f32_dpp v225, v225, v225 row_half_mirror row_mask:0xf bank_mask:0xf
	v_add_f32_dpp v226, v226, v226 row_half_mirror row_mask:0xf bank_mask:0xf
	v_add_f32_dpp v227, v227, v227 row_half_mirror row_mask:0xf bank_mask:0xf
	v_add_f32_dpp v220, v220, v220 row_mirror row_mask:0xf bank_mask:0xf
	v_add_f32_dpp v221, v221, v221 row_mirror row_mask:0xf bank_mask:0xf
	v_add_f32_dpp v222, v222, v222 row_mirror row_mask:0xf bank_mask:0xf
	v_add_f32_dpp v223, v223, v223 row_mirror row_mask:0xf bank_mask:0xf
	v_add_f32_dpp v224, v224, v224 row_mirror row_mask:0xf bank_mask:0xf
	v_add_f32_dpp v225, v225, v225 row_mirror row_mask:0xf bank_mask:0xf
	v_add_f32_dpp v226, v226, v226 row_mirror row_mask:0xf bank_mask:0xf
	v_add_f32_dpp v227, v227, v227 row_mirror row_mask:0xf bank_mask:0xf
	v_add_f32_dpp v220, v220, v220 row_bcast:15 row_mask:0xa bank_mask:0xf
	v_add_f32_dpp v221, v221, v221 row_bcast:15 row_mask:0xa bank_mask:0xf
	v_add_f32_dpp v222, v222, v222 row_bcast:15 row_mask:0xa bank_mask:0xf
	v_add_f32_dpp v223, v223, v223 row_bcast:15 row_mask:0xa bank_mask:0xf
	v_add_f32_dpp v224, v224, v224 row_bcast:15 row_mask:0xa bank_mask:0xf
	v_add_f32_dpp v225, v225, v225 row_bcast:15 row_mask:0xa bank_mask:0xf
	v_add_f32_dpp v226, v226, v226 row_bcast:15 row_mask:0xa bank_mask:0xf
	v_add_f32_dpp v227, v227, v227 row_bcast:15 row_mask:0xa bank_mask:0xf
	v_add_f32_dpp v220, v220, v220 row_bcast:31 row_mask:0xc bank_mask:0xf
	v_add_f32_dpp v221, v221, v221 row_bcast:31 row_mask:0xc bank_mask:0xf
	v_add_f32_dpp v222, v222, v222 row_bcast:31 row_mask:0xc bank_mask:0xf
	v_add_f32_dpp v223, v223, v223 row_bcast:31 row_mask:0xc bank_mask:0xf
	v_add_f32_dpp v224, v224, v224 row_bcast:31 row_mask:0xc bank_mask:0xf
	v_add_f32_dpp v225, v225, v225 row_bcast:31 row_mask:0xc bank_mask:0xf
	v_add_f32_dpp v226, v226, v226 row_bcast:31 row_mask:0xc bank_mask:0xf
	v_add_f32_dpp v227, v227, v227 row_bcast:31 row_mask:0xc bank_mask:0xf
	s_waitcnt vmcnt(0)
	v_mul_f32_e32 v228, v12, v188
	v_mul_f32_e32 v229, v28, v188
	v_mul_f32_e32 v230, v44, v188
	v_mul_f32_e32 v231, v60, v188
	v_mul_f32_e32 v232, v76, v188
	v_mul_f32_e32 v233, v92, v188
	v_mul_f32_e32 v234, v108, v188
	v_mul_f32_e32 v235, v124, v188
	v_fmac_f32_e32 v228, v13, v189
	v_fmac_f32_e32 v229, v29, v189
	v_fmac_f32_e32 v230, v45, v189
	v_fmac_f32_e32 v231, v61, v189
	v_fmac_f32_e32 v232, v77, v189
	v_fmac_f32_e32 v233, v93, v189
	v_fmac_f32_e32 v234, v109, v189
	v_fmac_f32_e32 v235, v125, v189
	v_fmac_f32_e32 v228, v14, v190
	v_fmac_f32_e32 v229, v30, v190
	v_fmac_f32_e32 v230, v46, v190
	v_fmac_f32_e32 v231, v62, v190
	v_fmac_f32_e32 v232, v78, v190
	v_fmac_f32_e32 v233, v94, v190
	v_fmac_f32_e32 v234, v110, v190
	v_fmac_f32_e32 v235, v126, v190
	v_fmac_f32_e32 v228, v15, v191
	v_fmac_f32_e32 v229, v31, v191
	v_fmac_f32_e32 v230, v47, v191
	v_fmac_f32_e32 v231, v63, v191
	v_fmac_f32_e32 v232, v79, v191
	v_fmac_f32_e32 v233, v95, v191
	v_fmac_f32_e32 v234, v111, v191
	v_fmac_f32_e32 v235, v127, v191
	v_fmac_f32_e32 v228, v16, v192
	v_fmac_f32_e32 v229, v32, v192
	v_fmac_f32_e32 v230, v48, v192
	v_fmac_f32_e32 v231, v64, v192
	v_fmac_f32_e32 v232, v80, v192
	v_fmac_f32_e32 v233, v96, v192
	v_fmac_f32_e32 v234, v112, v192
	v_fmac_f32_e32 v235, v128, v192
	v_fmac_f32_e32 v228, v17, v193
	v_fmac_f32_e32 v229, v33, v193
	v_fmac_f32_e32 v230, v49, v193
	v_fmac_f32_e32 v231, v65, v193
	v_fmac_f32_e32 v232, v81, v193
	v_fmac_f32_e32 v233, v97, v193
	v_fmac_f32_e32 v234, v113, v193
	v_fmac_f32_e32 v235, v129, v193
	v_fmac_f32_e32 v228, v18, v194
	v_fmac_f32_e32 v229, v34, v194
	v_fmac_f32_e32 v230, v50, v194
	v_fmac_f32_e32 v231, v66, v194
	v_fmac_f32_e32 v232, v82, v194
	v_fmac_f32_e32 v233, v98, v194
	v_fmac_f32_e32 v234, v114, v194
	v_fmac_f32_e32 v235, v130, v194
	v_fmac_f32_e32 v228, v19, v195
	v_fmac_f32_e32 v229, v35, v195
	v_fmac_f32_e32 v230, v51, v195
	v_fmac_f32_e32 v231, v67, v195
	v_fmac_f32_e32 v232, v83, v195
	v_fmac_f32_e32 v233, v99, v195
	v_fmac_f32_e32 v234, v115, v195
	v_fmac_f32_e32 v235, v131, v195
	v_fmac_f32_e32 v228, v20, v196
	v_fmac_f32_e32 v229, v36, v196
	v_fmac_f32_e32 v230, v52, v196
	v_fmac_f32_e32 v231, v68, v196
	v_fmac_f32_e32 v232, v84, v196
	v_fmac_f32_e32 v233, v100, v196
	v_fmac_f32_e32 v234, v116, v196
	v_fmac_f32_e32 v235, v132, v196
	v_fmac_f32_e32 v228, v21, v197
	v_fmac_f32_e32 v229, v37, v197
	v_fmac_f32_e32 v230, v53, v197
	v_fmac_f32_e32 v231, v69, v197
	v_fmac_f32_e32 v232, v85, v197
	v_fmac_f32_e32 v233, v101, v197
	v_fmac_f32_e32 v234, v117, v197
	v_fmac_f32_e32 v235, v133, v197
	v_fmac_f32_e32 v228, v22, v198
	v_fmac_f32_e32 v229, v38, v198
	v_fmac_f32_e32 v230, v54, v198
	v_fmac_f32_e32 v231, v70, v198
	v_fmac_f32_e32 v232, v86, v198
	v_fmac_f32_e32 v233, v102, v198
	v_fmac_f32_e32 v234, v118, v198
	v_fmac_f32_e32 v235, v134, v198
	v_fmac_f32_e32 v228, v23, v199
	v_fmac_f32_e32 v229, v39, v199
	v_fmac_f32_e32 v230, v55, v199
	v_fmac_f32_e32 v231, v71, v199
	v_fmac_f32_e32 v232, v87, v199
	v_fmac_f32_e32 v233, v103, v199
	v_fmac_f32_e32 v234, v119, v199
	v_fmac_f32_e32 v235, v135, v199
	v_fmac_f32_e32 v228, v24, v200
	v_fmac_f32_e32 v229, v40, v200
	v_fmac_f32_e32 v230, v56, v200
	v_fmac_f32_e32 v231, v72, v200
	v_fmac_f32_e32 v232, v88, v200
	v_fmac_f32_e32 v233, v104, v200
	v_fmac_f32_e32 v234, v120, v200
	v_fmac_f32_e32 v235, v136, v200
	v_fmac_f32_e32 v228, v25, v201
	v_fmac_f32_e32 v229, v41, v201
	v_fmac_f32_e32 v230, v57, v201
	v_fmac_f32_e32 v231, v73, v201
	v_fmac_f32_e32 v232, v89, v201
	v_fmac_f32_e32 v233, v105, v201
	v_fmac_f32_e32 v234, v121, v201
	v_fmac_f32_e32 v235, v137, v201
	v_fmac_f32_e32 v228, v26, v202
	v_fmac_f32_e32 v229, v42, v202
	v_fmac_f32_e32 v230, v58, v202
	v_fmac_f32_e32 v231, v74, v202
	v_fmac_f32_e32 v232, v90, v202
	v_fmac_f32_e32 v233, v106, v202
	v_fmac_f32_e32 v234, v122, v202
	v_fmac_f32_e32 v235, v138, v202
	v_fmac_f32_e32 v228, v27, v203
	v_fmac_f32_e32 v229, v43, v203
	v_fmac_f32_e32 v230, v59, v203
	v_fmac_f32_e32 v231, v75, v203
	v_fmac_f32_e32 v232, v91, v203
	v_fmac_f32_e32 v233, v107, v203
	v_fmac_f32_e32 v234, v123, v203
	v_fmac_f32_e32 v235, v139, v203
	s_nop 1
	v_add_f32_dpp v228, v228, v228 quad_perm:[1,0,3,2] row_mask:0xf bank_mask:0xf
	v_add_f32_dpp v229, v229, v229 quad_perm:[1,0,3,2] row_mask:0xf bank_mask:0xf
	v_add_f32_dpp v230, v230, v230 quad_perm:[1,0,3,2] row_mask:0xf bank_mask:0xf
	v_add_f32_dpp v231, v231, v231 quad_perm:[1,0,3,2] row_mask:0xf bank_mask:0xf
	v_add_f32_dpp v232, v232, v232 quad_perm:[1,0,3,2] row_mask:0xf bank_mask:0xf
	v_add_f32_dpp v233, v233, v233 quad_perm:[1,0,3,2] row_mask:0xf bank_mask:0xf
	v_add_f32_dpp v234, v234, v234 quad_perm:[1,0,3,2] row_mask:0xf bank_mask:0xf
	v_add_f32_dpp v235, v235, v235 quad_perm:[1,0,3,2] row_mask:0xf bank_mask:0xf
	v_add_f32_dpp v228, v228, v228 quad_perm:[2,3,0,1] row_mask:0xf bank_mask:0xf
	v_add_f32_dpp v229, v229, v229 quad_perm:[2,3,0,1] row_mask:0xf bank_mask:0xf
	v_add_f32_dpp v230, v230, v230 quad_perm:[2,3,0,1] row_mask:0xf bank_mask:0xf
	v_add_f32_dpp v231, v231, v231 quad_perm:[2,3,0,1] row_mask:0xf bank_mask:0xf
	v_add_f32_dpp v232, v232, v232 quad_perm:[2,3,0,1] row_mask:0xf bank_mask:0xf
	v_add_f32_dpp v233, v233, v233 quad_perm:[2,3,0,1] row_mask:0xf bank_mask:0xf
	v_add_f32_dpp v234, v234, v234 quad_perm:[2,3,0,1] row_mask:0xf bank_mask:0xf
	v_add_f32_dpp v235, v235, v235 quad_perm:[2,3,0,1] row_mask:0xf bank_mask:0xf
	v_add_f32_dpp v228, v228, v228 row_half_mirror row_mask:0xf bank_mask:0xf
	v_add_f32_dpp v229, v229, v229 row_half_mirror row_mask:0xf bank_mask:0xf
	v_add_f32_dpp v230, v230, v230 row_half_mirror row_mask:0xf bank_mask:0xf
	v_add_f32_dpp v231, v231, v231 row_half_mirror row_mask:0xf bank_mask:0xf
	v_add_f32_dpp v232, v232, v232 row_half_mirror row_mask:0xf bank_mask:0xf
	v_add_f32_dpp v233, v233, v233 row_half_mirror row_mask:0xf bank_mask:0xf
	v_add_f32_dpp v234, v234, v234 row_half_mirror row_mask:0xf bank_mask:0xf
	v_add_f32_dpp v235, v235, v235 row_half_mirror row_mask:0xf bank_mask:0xf
	v_add_f32_dpp v228, v228, v228 row_mirror row_mask:0xf bank_mask:0xf
	v_add_f32_dpp v229, v229, v229 row_mirror row_mask:0xf bank_mask:0xf
	v_add_f32_dpp v230, v230, v230 row_mirror row_mask:0xf bank_mask:0xf
	v_add_f32_dpp v231, v231, v231 row_mirror row_mask:0xf bank_mask:0xf
	v_add_f32_dpp v232, v232, v232 row_mirror row_mask:0xf bank_mask:0xf
	v_add_f32_dpp v233, v233, v233 row_mirror row_mask:0xf bank_mask:0xf
	v_add_f32_dpp v234, v234, v234 row_mirror row_mask:0xf bank_mask:0xf
	v_add_f32_dpp v235, v235, v235 row_mirror row_mask:0xf bank_mask:0xf
	v_add_f32_dpp v228, v228, v228 row_bcast:15 row_mask:0xa bank_mask:0xf
	v_add_f32_dpp v229, v229, v229 row_bcast:15 row_mask:0xa bank_mask:0xf
	v_add_f32_dpp v230, v230, v230 row_bcast:15 row_mask:0xa bank_mask:0xf
	v_add_f32_dpp v231, v231, v231 row_bcast:15 row_mask:0xa bank_mask:0xf
	v_add_f32_dpp v232, v232, v232 row_bcast:15 row_mask:0xa bank_mask:0xf
	v_add_f32_dpp v233, v233, v233 row_bcast:15 row_mask:0xa bank_mask:0xf
	v_add_f32_dpp v234, v234, v234 row_bcast:15 row_mask:0xa bank_mask:0xf
	v_add_f32_dpp v235, v235, v235 row_bcast:15 row_mask:0xa bank_mask:0xf
	v_add_f32_dpp v228, v228, v228 row_bcast:31 row_mask:0xc bank_mask:0xf
	v_add_f32_dpp v229, v229, v229 row_bcast:31 row_mask:0xc bank_mask:0xf
	v_add_f32_dpp v230, v230, v230 row_bcast:31 row_mask:0xc bank_mask:0xf
	v_add_f32_dpp v231, v231, v231 row_bcast:31 row_mask:0xc bank_mask:0xf
	v_add_f32_dpp v232, v232, v232 row_bcast:31 row_mask:0xc bank_mask:0xf
	v_add_f32_dpp v233, v233, v233 row_bcast:31 row_mask:0xc bank_mask:0xf
	v_add_f32_dpp v234, v234, v234 row_bcast:31 row_mask:0xc bank_mask:0xf
	v_add_f32_dpp v235, v235, v235 row_bcast:31 row_mask:0xc bank_mask:0xf
	v_cmp_eq_u32_e32 vcc, 0xfc0, v1
	s_and_saveexec_b64 s[24:25], vcc
	s_waitcnt lgkmcnt(0)
	v_add_f32_e32 v204, s16, v204
	v_add_f32_e32 v205, s17, v205
	v_add_f32_e32 v206, s18, v206
	v_add_f32_e32 v207, s19, v207
	v_add_f32_e32 v208, s20, v208
	v_add_f32_e32 v209, s21, v209
	v_add_f32_e32 v210, s22, v210
	v_add_f32_e32 v211, s23, v211
	v_add_f32_e32 v212, s16, v212
	v_add_f32_e32 v213, s17, v213
	v_add_f32_e32 v214, s18, v214
	v_add_f32_e32 v215, s19, v215
	v_add_f32_e32 v216, s20, v216
	v_add_f32_e32 v217, s21, v217
	v_add_f32_e32 v218, s22, v218
	v_add_f32_e32 v219, s23, v219
	v_add_f32_e32 v220, s16, v220
	v_add_f32_e32 v221, s17, v221
	v_add_f32_e32 v222, s18, v222
	v_add_f32_e32 v223, s19, v223
	v_add_f32_e32 v224, s20, v224
	v_add_f32_e32 v225, s21, v225
	v_add_f32_e32 v226, s22, v226
	v_add_f32_e32 v227, s23, v227
	v_add_f32_e32 v228, s16, v228
	v_add_f32_e32 v229, s17, v229
	v_add_f32_e32 v230, s18, v230
	v_add_f32_e32 v231, s19, v231
	v_add_f32_e32 v232, s20, v232
	v_add_f32_e32 v233, s21, v233
	v_add_f32_e32 v234, s22, v234
	v_add_f32_e32 v235, s23, v235
	v_mul_f32_e32 v204, 0x4038aa3b, v204
	v_mul_f32_e32 v205, 0x4038aa3b, v205
	v_mul_f32_e32 v206, 0x4038aa3b, v206
	v_mul_f32_e32 v207, 0x4038aa3b, v207
	v_mul_f32_e32 v208, 0x4038aa3b, v208
	v_mul_f32_e32 v209, 0x4038aa3b, v209
	v_mul_f32_e32 v210, 0x4038aa3b, v210
	v_mul_f32_e32 v211, 0x4038aa3b, v211
	v_mul_f32_e32 v212, 0x4038aa3b, v212
	v_mul_f32_e32 v213, 0x4038aa3b, v213
	v_mul_f32_e32 v214, 0x4038aa3b, v214
	v_mul_f32_e32 v215, 0x4038aa3b, v215
	v_mul_f32_e32 v216, 0x4038aa3b, v216
	v_mul_f32_e32 v217, 0x4038aa3b, v217
	v_mul_f32_e32 v218, 0x4038aa3b, v218
	v_mul_f32_e32 v219, 0x4038aa3b, v219
	v_mul_f32_e32 v220, 0x4038aa3b, v220
	v_mul_f32_e32 v221, 0x4038aa3b, v221
	v_mul_f32_e32 v222, 0x4038aa3b, v222
	v_mul_f32_e32 v223, 0x4038aa3b, v223
	v_mul_f32_e32 v224, 0x4038aa3b, v224
	v_mul_f32_e32 v225, 0x4038aa3b, v225
	v_mul_f32_e32 v226, 0x4038aa3b, v226
	v_mul_f32_e32 v227, 0x4038aa3b, v227
	v_mul_f32_e32 v228, 0x4038aa3b, v228
	v_mul_f32_e32 v229, 0x4038aa3b, v229
	v_mul_f32_e32 v230, 0x4038aa3b, v230
	v_mul_f32_e32 v231, 0x4038aa3b, v231
	v_mul_f32_e32 v232, 0x4038aa3b, v232
	v_mul_f32_e32 v233, 0x4038aa3b, v233
	v_mul_f32_e32 v234, 0x4038aa3b, v234
	v_mul_f32_e32 v235, 0x4038aa3b, v235
	global_store_dwordx4 v10, v[204:207], s[14:15]
	global_store_dwordx4 v10, v[208:211], s[14:15] offset:16
	v_add_u32_e32 v9, 0x1000, v10
	global_store_dwordx4 v9, v[212:215], s[14:15]
	global_store_dwordx4 v9, v[216:219], s[14:15] offset:16
	v_add_u32_e32 v8, 0x2000, v10
	global_store_dwordx4 v8, v[220:223], s[14:15]
	global_store_dwordx4 v8, v[224:227], s[14:15] offset:16
	v_add_u32_e32 v9, 0x3000, v10
	global_store_dwordx4 v9, v[228:231], s[14:15]
	global_store_dwordx4 v9, v[232:235], s[14:15] offset:16
	s_endpgm
